# post Q/K row loop software-pipelined: next iteration's 4 row loads issued at the top into spare registers, waits counted (vmcnt 4)
# speedup vs baseline: 1.0075x; 1.0003x over previous
.LBB0_766:
	s_mul_i32 s6, s73, 10
	s_add_i32 s46, s6, 3
	s_movk_i32 s6, 0x48
	s_ashr_i32 s7, s6, 31
	s_lshl_b64 s[6:7], s[6:7], 2
	s_add_u32 s6, s0, s6
	s_addc_u32 s7, s1, s7
	s_load_dwordx2 s[8:9], s[6:7], 0x0
	s_waitcnt lgkmcnt(0)
	s_cmp_le_i32 s8, s46
	s_cselect_b64 s[6:7], -1, 0
	s_cmp_lt_i32 s46, s9
	s_cselect_b64 s[8:9], -1, 0
	s_and_b64 s[6:7], s[6:7], s[8:9]
	s_andn2_b64 vcc, exec, s[6:7]
	s_cbranch_vccnz .LBB0_922
	s_waitcnt vmcnt(0)
	v_mbcnt_lo_u32_b32 v18, -1, 0
	v_mbcnt_hi_u32_b32 v18, -1, v18
	s_getreg_b32 s6, hwreg(HW_REG_HW_ID, 0, 6)
	s_lshl_b32 s6, s6, 2
	s_and_b32 s6, s6, 0xfc
	s_or_b32 s6, s6, 0x27100
	v_mov_b32_e32 v0, s6
	s_mov_b32 s6, 35
	ds_read_b32 v0, v0
	s_ashr_i32 s7, s6, 31
	s_lshl_b64 s[6:7], s[6:7], 3
	s_add_u32 s6, s0, s6
	s_addc_u32 s7, s1, s7
	s_load_dwordx2 s[20:21], s[6:7], 0x0
	v_bfe_u32 v52, v18, 2, 4
	s_waitcnt lgkmcnt(0)
	v_readfirstlane_b32 s8, v0
	v_cmp_lt_u32_e32 vcc, 5, v52
	s_load_dwordx2 s[10:11], s[0:1], 0xa8
	s_load_dwordx2 s[12:13], s[0:1], 0xb0
	s_waitcnt lgkmcnt(0)
	v_mov_b32_e32 v2, s10
	v_mov_b32_e32 v3, s11
	v_mov_b32_e32 v4, s12
	v_mov_b32_e32 v5, s13
	v_cndmask_b32_e32 v2, v2, v4, vcc
	v_cndmask_b32_e32 v3, v3, v5, vcc
	v_and_b32_e32 v19, 3, v18
	s_lshl_b32 s70, s73, 6
	v_lshlrev_b32_e32 v0, 6, v19
	s_mov_b32 s6, 35
	v_lshl_or_b32 v54, s8, 6, v18
	v_ashrrev_i32_e32 v55, 31, v54
	s_waitcnt vmcnt(0)
	v_lshl_add_u64 v[2:3], s[70:71], 2, v[2:3]
	v_lshl_add_u64 v[14:15], v[2:3], 0, v[0:1]
	global_load_dwordx4 v[2:5], v[14:15], off offset:48
	global_load_dwordx4 v[6:9], v[14:15], off offset:32
	global_load_dwordx4 v[10:13], v[14:15], off offset:16
	s_nop 0
	global_load_dwordx4 v[14:17], v[14:15], off
	s_barrier
	s_ashr_i32 s7, s6, 31
	s_lshl_b64 s[6:7], s[6:7], 3
	s_add_u32 s6, s0, s6
	s_addc_u32 s7, s1, s7
	s_load_dwordx2 s[6:7], s[6:7], 0x0
	v_lshl_add_u32 v0, v54, 4, 0
	s_waitcnt lgkmcnt(0)
	v_lshl_add_u64 v[20:21], v[54:55], 4, s[6:7]
	s_mov_b32 s6, 0x600000
	v_add_co_u32_e32 v20, vcc, s6, v20
	v_readlane_b32 s6, v254, 12
	s_nop 0
	v_addc_co_u32_e32 v21, vcc, 0, v21, vcc
	global_load_dwordx4 v[20:23], v[20:21], off
	s_waitcnt vmcnt(0)
	ds_write_b128 v0, v[20:23]
	v_ashrrev_i32_e32 v0, 5, v54
	v_and_b32_e32 v0, -2, v0
	v_add_u32_e32 v26, s6, v0
	s_mov_b32 s6, 0x8800
	v_cmp_gt_i32_e32 vcc, s6, v26
	s_waitcnt lgkmcnt(0)
	s_barrier
	s_and_saveexec_b64 s[22:23], vcc
	s_cbranch_execz .LBB0_806
	v_cmp_gt_u32_e64 s[6:7], 8, v52
	v_mov_b32_e32 v0, 0x380
	v_mov_b32_e32 v20, 0x300
	v_cndmask_b32_e64 v0, v0, v20, s[6:7]
	v_lshlrev_b32_e32 v22, 6, v52
	v_and_b32_e32 v18, 1, v18
	v_ashrrev_i32_e32 v27, 31, v26
	v_cmp_eq_u32_e64 s[10:11], 0, v18
	v_lshlrev_b64 v[20:21], 12, v[26:27]
	v_lshlrev_b32_e32 v18, 5, v19
	v_add_lshl_u32 v0, v0, v22, 1
	v_or3_b32 v20, v20, v18, v0
	v_lshlrev_b32_e32 v53, 4, v19
	v_cmp_gt_u32_e64 s[8:9], 2, v19
	v_cmp_lt_u32_e32 vcc, 13, v52
	v_lshl_add_u64 v[18:19], s[20:21], 0, v[20:21]
	s_mov_b64 s[12:13], 0x27801010
	v_cndmask_b32_e64 v55, 0, 8, vcc
	v_bfe_u32 v56, v54, 2, 1
	v_lshl_add_u64 v[28:29], v[18:19], 0, s[12:13]
	s_mov_b64 s[24:25], 0
	v_readlane_b32 s100, v255, 35
	v_readlane_b32 s101, v255, 36
	v_add_co_u32_e32 v112, vcc, 0xfffff000, v28
	s_nop 1
	v_addc_co_u32_e32 v113, vcc, -1, v29, vcc
	global_load_dwordx4 v[96:99], v[112:113], off offset:-16
	global_load_dwordx4 v[100:103], v[28:29], off offset:-4096
	global_load_dwordx4 v[104:107], v[28:29], off
	global_load_dwordx4 v[108:111], v[28:29], off offset:-16
	s_waitcnt vmcnt(0)
	s_branch .Lpq_go

.LBB0_774:
	s_waitcnt vmcnt(4)
.Lpq_go:
	v_mov_b32_e32 v36, v96
	v_mov_b32_e32 v37, v97
	v_mov_b32_e32 v38, v98
	v_mov_b32_e32 v39, v99
	v_mov_b32_e32 v44, v100
	v_mov_b32_e32 v45, v101
	v_mov_b32_e32 v46, v102
	v_mov_b32_e32 v47, v103
	v_mov_b32_e32 v18, v104
	v_mov_b32_e32 v19, v105
	v_mov_b32_e32 v20, v106
	v_mov_b32_e32 v21, v107
	v_mov_b32_e32 v22, v108
	v_mov_b32_e32 v23, v109
	v_mov_b32_e32 v24, v110
	v_mov_b32_e32 v25, v111
	v_add_u32_e32 v114, s66, v26
	s_mov_b32 s12, 0x87ff
	v_cmp_ge_i32_e32 vcc, s12, v114
	s_and_saveexec_b64 s[12:13], vcc
	s_cbranch_execz .Lpq_nopf
	v_lshl_add_u64 v[112:113], v[28:29], 0, s[100:101]
	v_add_co_u32_e32 v114, vcc, 0xfffff000, v112
	s_nop 1
	v_addc_co_u32_e32 v115, vcc, -1, v113, vcc
	global_load_dwordx4 v[96:99], v[114:115], off offset:-16
	global_load_dwordx4 v[100:103], v[112:113], off offset:-4096
	global_load_dwordx4 v[104:107], v[112:113], off
	global_load_dwordx4 v[108:111], v[112:113], off offset:-16
.Lpq_nopf:
	s_or_b64 exec, exec, s[12:13]
	v_lshlrev_b32_e32 v32, 16, v36
	v_and_b32_e32 v33, 0xffff0000, v36
	v_lshlrev_b32_e32 v34, 16, v37
	v_and_b32_e32 v35, 0xffff0000, v37
	v_lshlrev_b32_e32 v36, 16, v38
	v_and_b32_e32 v37, 0xffff0000, v38
	v_lshlrev_b32_e32 v38, 16, v39
	v_and_b32_e32 v39, 0xffff0000, v39
	v_lshlrev_b32_e32 v40, 16, v44
	v_and_b32_e32 v41, 0xffff0000, v44
	v_lshlrev_b32_e32 v42, 16, v45
	v_and_b32_e32 v43, 0xffff0000, v45
	v_lshlrev_b32_e32 v44, 16, v46
	v_and_b32_e32 v45, 0xffff0000, v46
	v_and_b32_e32 v30, 0xffff0000, v47
	v_lshlrev_b32_e32 v31, 16, v47
	s_and_saveexec_b64 s[12:13], s[6:7]
	s_cbranch_execz .LBB0_776
	v_pk_mul_f32 v[46:47], v[32:33], v[32:33]
	v_pk_mul_f32 v[48:49], v[34:35], v[34:35]
	v_add_f32_e32 v0, v46, v47
	v_add_f32_e32 v0, v48, v0
	v_pk_mul_f32 v[50:51], v[36:37], v[36:37]
	v_add_f32_e32 v0, v49, v0
	v_add_f32_e32 v0, v50, v0
	v_pk_mul_f32 v[58:59], v[38:39], v[38:39]
	v_add_f32_e32 v0, v51, v0
	v_add_f32_e32 v0, v58, v0
	v_pk_mul_f32 v[60:61], v[40:41], v[40:41]
	v_add_f32_e32 v0, v59, v0
	v_add_f32_e32 v0, v60, v0
	v_pk_mul_f32 v[62:63], v[42:43], v[42:43]
	v_add_f32_e32 v0, v61, v0
	v_add_f32_e32 v0, v62, v0
	v_pk_mul_f32 v[64:65], v[44:45], v[44:45]
	v_add_f32_e32 v0, v63, v0
	v_add_f32_e32 v0, v64, v0
	v_pk_mul_f32 v[66:67], v[30:31], v[30:31]
	v_add_f32_e32 v0, v65, v0
	v_add_f32_e32 v0, v67, v0
	v_add_f32_e32 v0, v66, v0
	v_mov_b32_e32 v46, 0x358637bd
	s_nop 0
	v_add_f32_dpp v0, v0, v0 quad_perm:[1,0,3,2] row_mask:0xf bank_mask:0xf bound_ctrl:1
	s_nop 1
	v_add_f32_dpp v0, v0, v0 quad_perm:[2,3,0,1] row_mask:0xf bank_mask:0xf bound_ctrl:1
	v_fmamk_f32 v0, v0, 0x3c800000, v46
	v_mul_f32_e32 v27, 0x4b800000, v0
	v_cmp_gt_f32_e32 vcc, s59, v0
	s_nop 1
	v_cndmask_b32_e32 v0, v0, v27, vcc
	v_rsq_f32_e32 v0, v0
	s_nop 0
	v_mul_f32_e32 v27, 0x45800000, v0
	v_cndmask_b32_e32 v0, v0, v27, vcc
	v_pk_mul_f32 v[30:31], v[0:1], v[30:31] op_sel_hi:[0,1]
	v_pk_mul_f32 v[32:33], v[0:1], v[32:33] op_sel_hi:[0,1]
	v_pk_mul_f32 v[34:35], v[0:1], v[34:35] op_sel_hi:[0,1]
	v_pk_mul_f32 v[36:37], v[0:1], v[36:37] op_sel_hi:[0,1]
	v_pk_mul_f32 v[38:39], v[0:1], v[38:39] op_sel_hi:[0,1]
	v_pk_mul_f32 v[40:41], v[0:1], v[40:41] op_sel_hi:[0,1]
	v_pk_mul_f32 v[42:43], v[0:1], v[42:43] op_sel_hi:[0,1]
	v_pk_mul_f32 v[44:45], v[0:1], v[44:45] op_sel_hi:[0,1]
	v_pk_mul_f32 v[46:47], v[4:5], v[30:31] op_sel:[0,1] op_sel_hi:[1,0]
	v_pk_mul_f32 v[32:33], v[14:15], v[32:33]
	v_pk_mul_f32 v[34:35], v[16:17], v[34:35]
	v_pk_mul_f32 v[36:37], v[10:11], v[36:37]
	v_pk_mul_f32 v[38:39], v[12:13], v[38:39]
	v_pk_mul_f32 v[40:41], v[6:7], v[40:41]
	v_pk_mul_f32 v[42:43], v[8:9], v[42:43]
	v_pk_mul_f32 v[44:45], v[2:3], v[44:45]
	v_mov_b32_e32 v31, v46
	v_mov_b32_e32 v30, v47

.LBB0_786:
	s_or_b64 exec, exec, s[26:27]
	v_cvt_pk_bf16_f32 v32, v32, v33
	v_cvt_pk_bf16_f32 v33, v34, v35
	v_cvt_pk_bf16_f32 v34, v36, v37
	v_cvt_pk_bf16_f32 v35, v38, v39
	v_cvt_pk_bf16_f32 v36, v40, v41
	v_cvt_pk_bf16_f32 v37, v42, v43
	v_cvt_pk_bf16_f32 v38, v44, v45
	v_cvt_pk_bf16_f32 v39, v46, v47
	global_store_dwordx4 v[50:51], v[32:35], off
	global_store_dwordx4 v[50:51], v[36:39], off offset:16
	v_and_b32_e32 v42, 0xffff0000, v21
	v_lshlrev_b32_e32 v32, 16, v22
	v_and_b32_e32 v33, 0xffff0000, v22
	v_lshlrev_b32_e32 v22, 16, v23
	v_and_b32_e32 v23, 0xffff0000, v23
	v_lshlrev_b32_e32 v34, 16, v24
	v_and_b32_e32 v35, 0xffff0000, v24
	v_lshlrev_b32_e32 v36, 16, v25
	v_and_b32_e32 v37, 0xffff0000, v25
	v_lshlrev_b32_e32 v24, 16, v18
	v_and_b32_e32 v25, 0xffff0000, v18
	v_lshlrev_b32_e32 v18, 16, v19
	v_and_b32_e32 v19, 0xffff0000, v19
	v_lshlrev_b32_e32 v38, 16, v20
	v_and_b32_e32 v39, 0xffff0000, v20
	v_lshlrev_b32_e32 v43, 16, v21
	s_and_saveexec_b64 s[26:27], s[6:7]
	s_cbranch_execz .LBB0_788
	v_pk_mul_f32 v[20:21], v[32:33], v[32:33]
	v_pk_mul_f32 v[40:41], v[22:23], v[22:23]
	v_add_f32_e32 v20, v20, v21
	v_add_f32_e32 v20, v40, v20
	v_pk_mul_f32 v[44:45], v[34:35], v[34:35]
	v_add_f32_e32 v20, v41, v20
	v_add_f32_e32 v20, v44, v20
	v_pk_mul_f32 v[46:47], v[36:37], v[36:37]
	v_add_f32_e32 v20, v45, v20
	v_add_f32_e32 v20, v46, v20
	v_pk_mul_f32 v[48:49], v[24:25], v[24:25]
	v_add_f32_e32 v20, v47, v20
	v_add_f32_e32 v20, v48, v20
	v_pk_mul_f32 v[50:51], v[18:19], v[18:19]
	v_add_f32_e32 v20, v49, v20
	v_add_f32_e32 v20, v50, v20
	v_pk_mul_f32 v[58:59], v[38:39], v[38:39]
	v_add_f32_e32 v20, v51, v20
	v_add_f32_e32 v20, v58, v20
	v_pk_mul_f32 v[60:61], v[42:43], v[42:43]
	v_add_f32_e32 v20, v59, v20
	v_add_f32_e32 v20, v61, v20
	v_add_f32_e32 v20, v60, v20
	v_mov_b32_e32 v40, 0x358637bd
	s_nop 0
	v_add_f32_dpp v20, v20, v20 quad_perm:[1,0,3,2] row_mask:0xf bank_mask:0xf bound_ctrl:1
	s_nop 1
	v_add_f32_dpp v20, v20, v20 quad_perm:[2,3,0,1] row_mask:0xf bank_mask:0xf bound_ctrl:1
	v_fmamk_f32 v20, v20, 0x3c800000, v40
	v_mul_f32_e32 v21, 0x4b800000, v20
	v_cmp_gt_f32_e64 s[18:19], s59, v20
	s_nop 1
	v_cndmask_b32_e64 v20, v20, v21, s[18:19]
	v_rsq_f32_e32 v20, v20
	s_nop 0
	v_mul_f32_e32 v21, 0x45800000, v20
	v_cndmask_b32_e64 v20, v20, v21, s[18:19]
	v_pk_mul_f32 v[32:33], v[20:21], v[32:33] op_sel_hi:[0,1]
	v_pk_mul_f32 v[22:23], v[20:21], v[22:23] op_sel_hi:[0,1]
	v_pk_mul_f32 v[34:35], v[20:21], v[34:35] op_sel_hi:[0,1]
	v_pk_mul_f32 v[36:37], v[20:21], v[36:37] op_sel_hi:[0,1]
	v_pk_mul_f32 v[24:25], v[20:21], v[24:25] op_sel_hi:[0,1]
	v_pk_mul_f32 v[18:19], v[20:21], v[18:19] op_sel_hi:[0,1]
	v_pk_mul_f32 v[38:39], v[20:21], v[38:39] op_sel_hi:[0,1]
	v_pk_mul_f32 v[20:21], v[20:21], v[42:43] op_sel_hi:[0,1]
	v_pk_mul_f32 v[20:21], v[4:5], v[20:21] op_sel:[0,1] op_sel_hi:[1,0]
	v_pk_mul_f32 v[32:33], v[14:15], v[32:33]
	v_pk_mul_f32 v[22:23], v[16:17], v[22:23]
	v_pk_mul_f32 v[34:35], v[10:11], v[34:35]
	v_pk_mul_f32 v[36:37], v[12:13], v[36:37]
	v_pk_mul_f32 v[24:25], v[6:7], v[24:25]
	v_pk_mul_f32 v[18:19], v[8:9], v[18:19]
	v_pk_mul_f32 v[38:39], v[2:3], v[38:39]
	v_mov_b32_e32 v43, v20
	v_mov_b32_e32 v42, v21
